# grid barrier: XCD leaders no longer bump the unused per-XCD relay word after release (one atomic + its wait less per barrier on 8 workgroups)
# baseline (speedup 1.0000x reference)
.LBB0_96:
	s_or_b64 exec, exec, s[10:11]
	s_waitcnt vmcnt(0)
	buffer_inv sc1
	s_waitcnt vmcnt(0)

.LBB0_407:
	s_or_b64 exec, exec, s[24:25]
	s_and_saveexec_b64 s[24:25], s[34:35]
	s_cbranch_execz .LBB0_409
	global_atomic_add v[2:3], v1, off
.LBB0_409:
	s_or_b64 exec, exec, s[24:25]
	s_waitcnt vmcnt(0)
	buffer_inv sc1
	s_waitcnt vmcnt(0)
.LBB0_410:
	s_or_b64 exec, exec, s[10:11]
	v_readlane_b32 s2, v255, 56
	v_readlane_b32 s3, v255, 57
	s_mov_b32 s3, s81
	v_writelane_b32 v255, s2, 56
	v_mov_b32_e32 v3, v0
	s_waitcnt lgkmcnt(0)
	v_writelane_b32 v255, s3, 57
	s_and_b64 s[2:3], s[30:31], exec
	s_barrier
	v_readlane_b32 s2, v253, 52
	v_ashrrev_i32_e32 v2, 6, v3
	s_cselect_b32 s95, 0x8200, s53
	v_add_u32_e32 v5, s2, v2
	v_cmp_gt_i32_e32 vcc, s95, v5
	s_and_saveexec_b64 s[24:25], vcc
	s_cbranch_execz .LBB0_425
	v_readlane_b32 s4, v255, 56
	v_readlane_b32 s5, v255, 57
	s_lshl_b64 s[2:3], s[4:5], 2
	v_readlane_b32 s52, v253, 0
	s_add_u32 s2, s96, s2
	v_readlane_b32 s58, v253, 6
	v_readlane_b32 s59, v253, 7
	s_addc_u32 s3, s97, s3
	v_mov_b32_e32 v2, 0x202000
	s_mov_b64 s[46:47], s[58:59]
	global_load_dword v2, v2, s[2:3]
	v_readlane_b32 s53, v253, 1
	s_add_u32 s2, s46, s0
	s_mov_b64 s[40:41], s[52:53]
	s_addc_u32 s3, s47, s1
	s_add_u32 s0, s40, s0
	v_and_b32_e32 v4, 63, v3
	s_addc_u32 s1, s41, s1
	v_lshlrev_b32_e32 v210, 2, v4
	global_load_dword v7, v210, s[0:1]
	v_cvt_f32_u32_e32 v3, s4
	v_readlane_b32 s4, v254, 40
	v_readlane_b32 s5, v254, 41
	v_mov_b32_e32 v23, v211
	v_lshlrev_b32_e32 v22, 1, v4
	v_lshl_add_u64 v[8:9], s[4:5], 0, v[210:211]
	v_readlane_b32 s4, v254, 52
	v_readlane_b32 s5, v254, 53
	v_mul_f32_e32 v3, 0xbe99999a, v3
	v_mul_f32_e32 v12, 0x3fb8aa3b, v3
	v_lshl_add_u64 v[10:11], s[4:5], 0, v[22:23]
	s_mov_b32 s4, 0x3fb8aa3b
	v_fma_f32 v13, v3, s4, -v12
	v_rndne_f32_e32 v14, v12
	v_fmac_f32_e32 v13, 0x32a5705f, v3
	v_sub_f32_e32 v12, v12, v14
	v_add_f32_e32 v12, v12, v13
	v_cvt_i32_f32_e32 v18, v14
	v_exp_f32_e32 v19, v12
	v_lshl_add_u64 v[16:17], s[0:1], 0, v[210:211]
	s_mov_b32 s0, 0xc2ce8ed0
	v_cmp_ngt_f32_e32 vcc, s0, v3
	v_ldexp_f32 v18, v19, v18
	s_mov_b32 s0, 0x42b17218
	v_readlane_b32 s54, v253, 2
	v_readlane_b32 s55, v253, 3
	v_cndmask_b32_e32 v18, 0, v18, vcc
	v_cmp_nlt_f32_e32 vcc, s0, v3
	v_readlane_b32 s64, v253, 12
	v_readlane_b32 s65, v253, 13
	v_readlane_b32 s66, v253, 14
	v_readlane_b32 s67, v253, 15
	v_readlane_b32 s54, v255, 35
	v_readlane_b32 s4, v254, 50
	v_cndmask_b32_e32 v3, v225, v18, vcc
	v_mov_b32_e32 v18, 0xbf4ccccd
	v_readlane_b32 s6, v254, 46
	v_readlane_b32 s64, v255, 43
	v_readlane_b32 s66, v255, 37
	v_readlane_b32 s55, v255, 36
	v_readlane_b32 s46, v255, 41
	v_readlane_b32 s5, v254, 51
	v_fmamk_f32 v3, v3, 0x3f19999a, v18
	v_readlane_b32 s7, v254, 47
	v_readlane_b32 s65, v255, 44
	s_mov_b32 s42, 0x8200000
	s_mov_b32 s53, 0x8000
	s_movk_i32 s33, 0x2c00
	v_readlane_b32 s67, v255, 38
	v_readlane_b32 s47, v255, 42
	v_or_b32_e32 v6, 0x80, v4
	v_lshl_add_u64 v[12:13], s[4:5], 0, v[210:211]
	v_lshl_add_u64 v[14:15], s[2:3], 0, v[210:211]
	v_add_f32_e32 v19, 1.0, v3
	v_or_b32_e32 v18, 0x100, v4
	v_or_b32_e32 v20, 0x180, v4
	v_lshl_add_u64 v[22:23], s[54:55], 0, v[22:23]
	s_mov_b64 s[10:11], 0
	v_readlane_b32 s56, v253, 4
	v_readlane_b32 s57, v253, 5
	v_readlane_b32 s60, v253, 8
	v_readlane_b32 s61, v253, 9
	v_readlane_b32 s62, v253, 10
	v_readlane_b32 s63, v253, 11
	s_waitcnt vmcnt(1)
	v_mov_b32_e32 v3, v2
	s_branch .LBB0_413
